# staged bias-init waits combined with the earlier-issued final layer-2 MFMA on top of the tail LDS reorder
# speedup vs baseline: 1.0075x; 1.0016x over previous
.LBB1_4:
	s_and_saveexec_b64 s[8:9], s[2:3]
	v_perm_b32 v5, v1, v102, s23
	v_perm_b32 v9, v121, v103, s23
	s_or_b64 exec, exec, s[8:9]
	v_mov_b32_e32 v144, v1
	v_mov_b32_e32 v145, v121
	v_mfma_f32_16x16x32_f16 v[164:167], v[30:33], v[2:5], 0
	v_mfma_f32_16x16x32_f16 v[180:183], v[22:25], v[2:5], 0
	s_cmp_lg_u32 s22, 0x818000
	v_permlane32_swap_b32_e32 v1, v144
	v_permlane32_swap_b32_e32 v121, v145
	v_mfma_f32_16x16x32_f16 v[168:171], v[30:33], v[6:9], 0
	v_mfma_f32_16x16x32_f16 v[184:187], v[22:25], v[6:9], 0
	s_cselect_b32 s9, s11, 15
	s_and_saveexec_b64 s[32:33], s[2:3]
	v_perm_b32 v17, v144, v115, s23
	v_perm_b32 v29, v145, v116, s23
	s_or_b64 exec, exec, s[32:33]
	v_mfma_f32_16x16x32_f16 v[172:175], v[30:33], v[14:17], 0
	v_mfma_f32_16x16x32_f16 v[188:191], v[22:25], v[14:17], 0
	v_mfma_f32_16x16x32_f16 v[176:179], v[30:33], v[26:29], 0
	v_mfma_f32_16x16x32_f16 v[192:195], v[22:25], v[26:29], 0
	v_mfma_f32_16x16x32_f16 v[208:211], v[18:21], v[2:5], 0
	v_mfma_f32_16x16x32_f16 v[224:227], v[10:13], v[2:5], 0
	v_cvt_pk_f16_f32 v122, v164, v165
	v_cvt_pk_f16_f32 v123, v166, v167
	v_pk_max_f16 v122, v122, 0
	v_pk_max_f16 v123, v123, 0
	v_cvt_pk_f16_f32 v124, v180, v181
	v_cvt_pk_f16_f32 v125, v182, v183
	v_pk_max_f16 v124, v124, 0
	v_pk_max_f16 v125, v125, 0
	ds_write_b128 v107, v[122:125]
	v_mfma_f32_16x16x32_f16 v[212:215], v[18:21], v[6:9], 0
	v_mfma_f32_16x16x32_f16 v[228:231], v[10:13], v[6:9], 0
	v_cvt_pk_f16_f32 v126, v168, v169
	v_cvt_pk_f16_f32 v127, v170, v171
	v_pk_max_f16 v126, v126, 0
	v_pk_max_f16 v127, v127, 0
	v_cvt_pk_f16_f32 v128, v184, v185
	v_cvt_pk_f16_f32 v129, v186, v187
	v_pk_max_f16 v128, v128, 0
	v_pk_max_f16 v129, v129, 0
	ds_write_b128 v107, v[126:129] offset:16384
	v_mfma_f32_16x16x32_f16 v[216:219], v[18:21], v[14:17], 0
	v_mfma_f32_16x16x32_f16 v[232:235], v[10:13], v[14:17], 0
	v_cvt_pk_f16_f32 v134, v172, v173
	v_cvt_pk_f16_f32 v135, v174, v175
	v_pk_max_f16 v134, v134, 0
	v_pk_max_f16 v135, v135, 0
	v_cvt_pk_f16_f32 v136, v188, v189
	v_cvt_pk_f16_f32 v137, v190, v191
	v_pk_max_f16 v136, v136, 0
	v_pk_max_f16 v137, v137, 0
	ds_write_b128 v107, v[134:137] offset:32768
	v_mfma_f32_16x16x32_f16 v[220:223], v[18:21], v[26:29], 0
	v_mfma_f32_16x16x32_f16 v[236:239], v[10:13], v[26:29], 0
	v_cvt_pk_f16_f32 v138, v176, v177
	v_cvt_pk_f16_f32 v139, v178, v179
	v_pk_max_f16 v138, v138, 0
	v_pk_max_f16 v139, v139, 0
	v_cvt_pk_f16_f32 v140, v192, v193
	v_cvt_pk_f16_f32 v141, v194, v195
	v_pk_max_f16 v140, v140, 0
	v_pk_max_f16 v141, v141, 0
	ds_write_b128 v107, v[138:141] offset:49152
	v_add_u32_e32 v111, s64, v111
	v_add_u32_e32 v98, s65, v98
	s_lshl_b32 s20, s9, 7
	v_lshl_add_u64 v[0:1], s[20:21], 3, v[132:133]
	s_add_i32 s25, s22, s34
	s_lshl_b32 s8, s9, 8
	buffer_load_dwordx4 v[192:195], v147, s[16:19], s25 offen
	buffer_load_dwordx4 v[196:199], v148, s[16:19], s25 offen
	buffer_load_dwordx4 v[200:203], v149, s[16:19], s25 offen
	buffer_load_dwordx4 v[204:207], v150, s[16:19], s25 offen
	s_waitcnt vmcnt(19) lgkmcnt(8)
	v_mfma_f32_16x16x32_f16 v[164:167], v[58:61], v[122:125], v[240:243]
	v_cvt_pk_f16_f32 v142, v208, v209
	v_cvt_pk_f16_f32 v143, v210, v211
	v_mfma_f32_16x16x32_f16 v[168:171], v[58:61], v[126:129], v[240:243]
	v_pk_max_f16 v142, v142, 0
	v_pk_max_f16 v143, v143, 0
	v_mfma_f32_16x16x32_f16 v[172:175], v[58:61], v[134:137], v[240:243]
	v_cvt_pk_f16_f32 v144, v224, v225
	v_cvt_pk_f16_f32 v145, v226, v227
	v_mfma_f32_16x16x32_f16 v[10:13], v[58:61], v[138:141], v[240:243]
	v_pk_max_f16 v144, v144, 0
	v_pk_max_f16 v145, v145, 0
	ds_write_b128 v108, v[142:145]
	s_waitcnt vmcnt(18) lgkmcnt(8)
	v_mfma_f32_16x16x32_f16 v[58:61], v[54:57], v[122:125], v[244:247]
	v_cvt_pk_f16_f32 v152, v212, v213
	v_cvt_pk_f16_f32 v153, v214, v215
	v_mfma_f32_16x16x32_f16 v[176:179], v[54:57], v[126:129], v[244:247]
	v_pk_max_f16 v152, v152, 0
	v_pk_max_f16 v153, v153, 0
	v_mfma_f32_16x16x32_f16 v[180:183], v[54:57], v[134:137], v[244:247]
	v_cvt_pk_f16_f32 v154, v228, v229
	v_cvt_pk_f16_f32 v155, v230, v231
	v_mfma_f32_16x16x32_f16 v[18:21], v[54:57], v[138:141], v[244:247]
	v_pk_max_f16 v154, v154, 0
	v_pk_max_f16 v155, v155, 0
	ds_write_b128 v108, v[152:155] offset:16384
	s_waitcnt vmcnt(17) lgkmcnt(8)
	v_mfma_f32_16x16x32_f16 v[54:57], v[50:53], v[122:125], v[248:251]
	v_cvt_pk_f16_f32 v156, v216, v217
	v_cvt_pk_f16_f32 v157, v218, v219
	v_mfma_f32_16x16x32_f16 v[184:187], v[50:53], v[126:129], v[248:251]
	v_pk_max_f16 v156, v156, 0
	v_pk_max_f16 v157, v157, 0
	v_mfma_f32_16x16x32_f16 v[188:191], v[50:53], v[134:137], v[248:251]
	v_cvt_pk_f16_f32 v158, v232, v233
	v_cvt_pk_f16_f32 v159, v234, v235
	v_mfma_f32_16x16x32_f16 v[22:25], v[50:53], v[138:141], v[248:251]
	v_pk_max_f16 v158, v158, 0
	v_pk_max_f16 v159, v159, 0
	ds_write_b128 v108, v[156:159] offset:32768
	s_waitcnt vmcnt(16) lgkmcnt(8)
	v_mfma_f32_16x16x32_f16 v[50:53], v[38:41], v[122:125], v[252:255]
	s_load_dword s30, s[12:13], 0x0
	v_cvt_pk_f16_f32 v160, v220, v221
	v_cvt_pk_f16_f32 v161, v222, v223
	v_mfma_f32_16x16x32_f16 v[122:125], v[38:41], v[126:129], v[252:255]
	v_pk_max_f16 v160, v160, 0
	v_pk_max_f16 v161, v161, 0
	v_mfma_f32_16x16x32_f16 v[126:129], v[38:41], v[134:137], v[252:255]
	v_cvt_pk_f16_f32 v162, v236, v237
	v_cvt_pk_f16_f32 v163, v238, v239
	v_mfma_f32_16x16x32_f16 v[38:41], v[38:41], v[138:141], v[252:255]
	v_pk_max_f16 v162, v162, 0
	v_pk_max_f16 v163, v163, 0
	ds_write_b128 v108, v[160:163] offset:49152
	s_add_i32 s9, s22, s35
	s_waitcnt vmcnt(15)
	v_mfma_f32_16x16x32_f16 v[164:167], v[94:97], v[142:145], v[164:167]
	v_mfma_f32_16x16x32_f16 v[168:171], v[94:97], v[152:155], v[168:171]
	s_waitcnt vmcnt(14)
	v_mfma_f32_16x16x32_f16 v[58:61], v[90:93], v[142:145], v[58:61]
	v_mfma_f32_16x16x32_f16 v[176:179], v[90:93], v[152:155], v[176:179]
	s_waitcnt vmcnt(13)
	v_mfma_f32_16x16x32_f16 v[54:57], v[78:81], v[142:145], v[54:57]
	v_mfma_f32_16x16x32_f16 v[184:187], v[78:81], v[152:155], v[184:187]
	s_waitcnt vmcnt(12)
	v_mfma_f32_16x16x32_f16 v[50:53], v[34:37], v[142:145], v[50:53]
	buffer_load_dwordx4 v[140:143], v147, s[16:19], s9 offen
	buffer_load_dwordx4 v[220:223], v148, s[16:19], s9 offen
	v_mfma_f32_16x16x32_f16 v[122:125], v[34:37], v[152:155], v[122:125]
	buffer_load_dwordx4 v[152:155], v149, s[16:19], s9 offen
	buffer_load_dwordx4 v[224:227], v150, s[16:19], s9 offen
	s_mov_b32 s9, s21
	s_waitcnt lgkmcnt(0)
	s_barrier
	v_add_u32_e32 v99, s66, v99
	ds_read_b128 v[136:139], v99
	ds_read_b128 v[208:211], v99 offset:16384
	ds_read_b128 v[212:215], v99 offset:32768
	ds_read_b128 v[216:219], v99 offset:49152
	v_mfma_f32_16x16x32_f16 v[172:175], v[94:97], v[156:159], v[172:175]
	v_mfma_f32_16x16x32_f16 v[94:97], v[94:97], v[160:163], v[10:13]
	s_nop 2
	v_lshl_add_u64 v[10:11], s[8:9], 4, v[130:131]
	v_mfma_f32_16x16x32_f16 v[180:183], v[90:93], v[156:159], v[180:183]
	v_mfma_f32_16x16x32_f16 v[90:93], v[90:93], v[160:163], v[18:21]
	v_mfma_f32_16x16x32_f16 v[188:191], v[78:81], v[156:159], v[188:191]
	v_mfma_f32_16x16x32_f16 v[78:81], v[78:81], v[160:163], v[22:25]
	global_load_dwordx4 v[30:33], v[10:11], off
	s_nop 1
	global_load_dwordx4 v[22:25], v[10:11], off offset:1024
	global_load_dwordx4 v[18:21], v[10:11], off offset:2048
	s_nop 0
	global_load_dwordx4 v[10:13], v[10:11], off offset:3072
	s_nop 0
	global_load_dwordx2 v[134:135], v[0:1], off
	v_mfma_f32_16x16x32_f16 v[126:129], v[34:37], v[156:159], v[126:129]
	v_mfma_f32_16x16x32_f16 v[34:37], v[34:37], v[160:163], v[38:41]
	s_nop 2
	v_add_u32_e32 v100, s67, v100
	ds_read_b128 v[38:41], v100
	ds_read_b128 v[156:159], v100 offset:16384
	ds_read_b128 v[160:163], v100 offset:32768
	ds_read_b128 v[228:231], v100 offset:49152
	s_add_i32 s8, s22, s36
	s_waitcnt vmcnt(20) lgkmcnt(7)
	v_mfma_f32_16x16x32_f16 v[164:167], v[82:85], v[136:139], v[164:167]
	s_waitcnt lgkmcnt(6)
	v_mfma_f32_16x16x32_f16 v[168:171], v[82:85], v[208:211], v[168:171]
	s_waitcnt lgkmcnt(5)
	v_mfma_f32_16x16x32_f16 v[172:175], v[82:85], v[212:215], v[172:175]
	s_waitcnt lgkmcnt(4)
	v_mfma_f32_16x16x32_f16 v[82:85], v[82:85], v[216:219], v[94:97]
	s_waitcnt vmcnt(19)
	v_mfma_f32_16x16x32_f16 v[58:61], v[70:73], v[136:139], v[58:61]
	v_mfma_f32_16x16x32_f16 v[94:97], v[70:73], v[208:211], v[176:179]
	v_mfma_f32_16x16x32_f16 v[176:179], v[70:73], v[212:215], v[180:183]
	v_mfma_f32_16x16x32_f16 v[70:73], v[70:73], v[216:219], v[90:93]
	s_waitcnt vmcnt(18)
	v_mfma_f32_16x16x32_f16 v[54:57], v[62:65], v[136:139], v[54:57]
	v_mfma_f32_16x16x32_f16 v[90:93], v[62:65], v[208:211], v[184:187]
	v_mfma_f32_16x16x32_f16 v[180:183], v[62:65], v[212:215], v[188:191]
	v_mfma_f32_16x16x32_f16 v[62:65], v[62:65], v[216:219], v[78:81]
	s_waitcnt vmcnt(17)
	v_mfma_f32_16x16x32_f16 v[50:53], v[42:45], v[136:139], v[50:53]
	v_mfma_f32_16x16x32_f16 v[78:81], v[42:45], v[208:211], v[122:125]
	v_mfma_f32_16x16x32_f16 v[122:125], v[42:45], v[212:215], v[126:129]
	s_nop 2
	buffer_load_dwordx4 v[126:129], v147, s[16:19], s8 offen
	buffer_load_dwordx4 v[136:139], v148, s[16:19], s8 offen
	buffer_load_dwordx4 v[184:187], v149, s[16:19], s8 offen
	buffer_load_dwordx4 v[188:191], v150, s[16:19], s8 offen
	v_mfma_f32_16x16x32_f16 v[34:37], v[42:45], v[216:219], v[34:37]
	v_add_u32_e32 v111, s68, v111
	ds_read_b128 v[42:45], v111
	ds_read_b128 v[208:211], v111 offset:16384
	ds_read_b128 v[212:215], v111 offset:32768
	ds_read_b128 v[216:219], v111 offset:49152
	s_add_i32 s8, s22, s37
	s_waitcnt vmcnt(20) lgkmcnt(7)
	v_mfma_f32_16x16x32_f16 v[164:167], v[86:89], v[38:41], v[164:167]
	s_waitcnt lgkmcnt(6)
	v_mfma_f32_16x16x32_f16 v[168:171], v[86:89], v[156:159], v[168:171]
	s_waitcnt lgkmcnt(5)
	v_mfma_f32_16x16x32_f16 v[172:175], v[86:89], v[160:163], v[172:175]
	s_waitcnt lgkmcnt(4)
	v_mfma_f32_16x16x32_f16 v[82:85], v[86:89], v[228:231], v[82:85]
	s_waitcnt vmcnt(19)
	v_mfma_f32_16x16x32_f16 v[58:61], v[74:77], v[38:41], v[58:61]
	v_mfma_f32_16x16x32_f16 v[86:89], v[74:77], v[156:159], v[94:97]
	v_mfma_f32_16x16x32_f16 v[94:97], v[74:77], v[160:163], v[176:179]
	v_mfma_f32_16x16x32_f16 v[70:73], v[74:77], v[228:231], v[70:73]
	s_waitcnt vmcnt(18)
	v_mfma_f32_16x16x32_f16 v[54:57], v[66:69], v[38:41], v[54:57]
	v_mfma_f32_16x16x32_f16 v[74:77], v[66:69], v[156:159], v[90:93]
	v_mfma_f32_16x16x32_f16 v[90:93], v[66:69], v[160:163], v[180:183]
	v_mfma_f32_16x16x32_f16 v[62:65], v[66:69], v[228:231], v[62:65]
	s_waitcnt vmcnt(17)
	v_mfma_f32_16x16x32_f16 v[38:41], v[46:49], v[38:41], v[50:53]
	v_mfma_f32_16x16x32_f16 v[50:53], v[46:49], v[156:159], v[78:81]
	v_mfma_f32_16x16x32_f16 v[66:69], v[46:49], v[160:163], v[122:125]
	s_nop 1
	buffer_load_dwordx4 v[78:81], v147, s[16:19], s8 offen
	buffer_load_dwordx4 v[122:125], v148, s[16:19], s8 offen
	buffer_load_dwordx4 v[156:159], v149, s[16:19], s8 offen
	buffer_load_dwordx4 v[160:163], v150, s[16:19], s8 offen
	v_mfma_f32_16x16x32_f16 v[34:37], v[46:49], v[228:231], v[34:37]
	v_add_u32_e32 v98, s69, v98
	ds_read_b128 v[46:49], v98
	ds_read_b128 v[176:179], v98 offset:16384
	ds_read_b128 v[180:183], v98 offset:32768
	ds_read_b128 v[228:231], v98 offset:49152
	s_add_i32 s8, s22, s38
	s_waitcnt vmcnt(20) lgkmcnt(7)
	v_mfma_f32_16x16x32_f16 v[164:167], v[192:195], v[42:45], v[164:167]
	s_waitcnt lgkmcnt(6)
	v_mfma_f32_16x16x32_f16 v[168:171], v[192:195], v[208:211], v[168:171]
	s_waitcnt lgkmcnt(5)
	v_mfma_f32_16x16x32_f16 v[172:175], v[192:195], v[212:215], v[172:175]
	s_waitcnt lgkmcnt(4)
	v_mfma_f32_16x16x32_f16 v[82:85], v[192:195], v[216:219], v[82:85]
	s_waitcnt vmcnt(19)
	v_mfma_f32_16x16x32_f16 v[58:61], v[196:199], v[42:45], v[58:61]
	v_mfma_f32_16x16x32_f16 v[86:89], v[196:199], v[208:211], v[86:89]
	v_mfma_f32_16x16x32_f16 v[94:97], v[196:199], v[212:215], v[94:97]
	v_mfma_f32_16x16x32_f16 v[70:73], v[196:199], v[216:219], v[70:73]
	s_waitcnt vmcnt(18)
	v_mfma_f32_16x16x32_f16 v[54:57], v[200:203], v[42:45], v[54:57]
	v_mfma_f32_16x16x32_f16 v[74:77], v[200:203], v[208:211], v[74:77]
	v_mfma_f32_16x16x32_f16 v[90:93], v[200:203], v[212:215], v[90:93]
	v_mfma_f32_16x16x32_f16 v[62:65], v[200:203], v[216:219], v[62:65]
	s_waitcnt vmcnt(17)
	v_mfma_f32_16x16x32_f16 v[38:41], v[204:207], v[42:45], v[38:41]
	v_mfma_f32_16x16x32_f16 v[42:45], v[204:207], v[208:211], v[50:53]
	v_mfma_f32_16x16x32_f16 v[50:53], v[204:207], v[212:215], v[66:69]
	s_nop 2
	buffer_load_dwordx4 v[66:69], v147, s[16:19], s8 offen
	buffer_load_dwordx4 v[192:195], v148, s[16:19], s8 offen
	buffer_load_dwordx4 v[196:199], v149, s[16:19], s8 offen
	buffer_load_dwordx4 v[200:203], v150, s[16:19], s8 offen
	v_mfma_f32_16x16x32_f16 v[34:37], v[204:207], v[216:219], v[34:37]
	v_add_u32_e32 v99, s70, v99
	ds_read_b128 v[204:207], v99
	ds_read_b128 v[208:211], v99 offset:16384
	ds_read_b128 v[212:215], v99 offset:32768
	ds_read_b128 v[216:219], v99 offset:49152
	s_add_i32 s8, s22, s39
	s_waitcnt vmcnt(20) lgkmcnt(7)
	v_mfma_f32_16x16x32_f16 v[164:167], v[140:143], v[46:49], v[164:167]
	s_waitcnt lgkmcnt(6)
	v_mfma_f32_16x16x32_f16 v[168:171], v[140:143], v[176:179], v[168:171]
	s_waitcnt lgkmcnt(5)
	v_mfma_f32_16x16x32_f16 v[172:175], v[140:143], v[180:183], v[172:175]
	s_waitcnt lgkmcnt(4)
	v_mfma_f32_16x16x32_f16 v[82:85], v[140:143], v[228:231], v[82:85]
	s_waitcnt vmcnt(19)
	v_mfma_f32_16x16x32_f16 v[58:61], v[220:223], v[46:49], v[58:61]
	v_mfma_f32_16x16x32_f16 v[86:89], v[220:223], v[176:179], v[86:89]
	s_waitcnt vmcnt(18)
	v_mfma_f32_16x16x32_f16 v[54:57], v[152:155], v[46:49], v[54:57]
	v_mfma_f32_16x16x32_f16 v[74:77], v[152:155], v[176:179], v[74:77]
	v_mfma_f32_16x16x32_f16 v[90:93], v[152:155], v[180:183], v[90:93]
	v_mfma_f32_16x16x32_f16 v[62:65], v[152:155], v[228:231], v[62:65]
	s_waitcnt vmcnt(17)
	v_mfma_f32_16x16x32_f16 v[38:41], v[224:227], v[46:49], v[38:41]
	v_mfma_f32_16x16x32_f16 v[42:45], v[224:227], v[176:179], v[42:45]
	v_mfma_f32_16x16x32_f16 v[46:49], v[224:227], v[180:183], v[50:53]
	s_nop 2
	buffer_load_dwordx4 v[50:53], v147, s[16:19], s8 offen
	buffer_load_dwordx4 v[140:143], v148, s[16:19], s8 offen
	buffer_load_dwordx4 v[152:155], v149, s[16:19], s8 offen
	buffer_load_dwordx4 v[176:179], v150, s[16:19], s8 offen
	v_mfma_f32_16x16x32_f16 v[94:97], v[220:223], v[180:183], v[94:97]
	v_mfma_f32_16x16x32_f16 v[70:73], v[220:223], v[228:231], v[70:73]
	v_mfma_f32_16x16x32_f16 v[34:37], v[224:227], v[228:231], v[34:37]
	v_add_u32_e32 v100, s71, v100
	ds_read_b128 v[180:183], v100
	ds_read_b128 v[220:223], v100 offset:16384
	ds_read_b128 v[224:227], v100 offset:32768
	ds_read_b128 v[228:231], v100 offset:49152
	s_add_i32 s8, s22, s40
	s_waitcnt vmcnt(15) lgkmcnt(7)
	v_mfma_f32_16x16x32_f16 v[164:167], v[126:129], v[204:207], v[164:167]
	s_waitcnt lgkmcnt(6)
	v_mfma_f32_16x16x32_f16 v[168:171], v[126:129], v[208:211], v[168:171]
	s_waitcnt lgkmcnt(5)
	v_mfma_f32_16x16x32_f16 v[172:175], v[126:129], v[212:215], v[172:175]
	s_waitcnt lgkmcnt(4)
	v_mfma_f32_16x16x32_f16 v[82:85], v[126:129], v[216:219], v[82:85]
	s_waitcnt vmcnt(14)
	v_mfma_f32_16x16x32_f16 v[58:61], v[136:139], v[204:207], v[58:61]
	v_mfma_f32_16x16x32_f16 v[86:89], v[136:139], v[208:211], v[86:89]
	v_mfma_f32_16x16x32_f16 v[94:97], v[136:139], v[212:215], v[94:97]
	v_mfma_f32_16x16x32_f16 v[70:73], v[136:139], v[216:219], v[70:73]
	s_waitcnt vmcnt(13)
	v_mfma_f32_16x16x32_f16 v[54:57], v[184:187], v[204:207], v[54:57]
	v_mfma_f32_16x16x32_f16 v[74:77], v[184:187], v[208:211], v[74:77]
	v_mfma_f32_16x16x32_f16 v[90:93], v[184:187], v[212:215], v[90:93]
	v_mfma_f32_16x16x32_f16 v[62:65], v[184:187], v[216:219], v[62:65]
	s_waitcnt vmcnt(12)
	v_mfma_f32_16x16x32_f16 v[38:41], v[188:191], v[204:207], v[38:41]
	buffer_load_dwordx4 v[126:129], v147, s[16:19], s8 offen
	buffer_load_dwordx4 v[136:139], v148, s[16:19], s8 offen
	buffer_load_dwordx4 v[184:187], v149, s[16:19], s8 offen
	buffer_load_dwordx4 v[204:207], v150, s[16:19], s8 offen
	v_mfma_f32_16x16x32_f16 v[42:45], v[188:191], v[208:211], v[42:45]
	v_mfma_f32_16x16x32_f16 v[46:49], v[188:191], v[212:215], v[46:49]
	v_mfma_f32_16x16x32_f16 v[34:37], v[188:191], v[216:219], v[34:37]
	v_add_u32_e32 v111, s72, v111
	ds_read_b128 v[188:191], v111
	ds_read_b128 v[208:211], v111 offset:16384
	ds_read_b128 v[212:215], v111 offset:32768
	ds_read_b128 v[216:219], v111 offset:49152
	s_add_i32 s8, s22, s41
	s_waitcnt vmcnt(15) lgkmcnt(7)
	v_mfma_f32_16x16x32_f16 v[164:167], v[78:81], v[180:183], v[164:167]
	s_waitcnt lgkmcnt(6)
	v_mfma_f32_16x16x32_f16 v[168:171], v[78:81], v[220:223], v[168:171]
	s_waitcnt lgkmcnt(5)
	v_mfma_f32_16x16x32_f16 v[172:175], v[78:81], v[224:227], v[172:175]
	s_waitcnt lgkmcnt(4)
	v_mfma_f32_16x16x32_f16 v[78:81], v[78:81], v[228:231], v[82:85]
	s_waitcnt vmcnt(14)
	v_mfma_f32_16x16x32_f16 v[58:61], v[122:125], v[180:183], v[58:61]
	v_mfma_f32_16x16x32_f16 v[82:85], v[122:125], v[220:223], v[86:89]
	v_mfma_f32_16x16x32_f16 v[86:89], v[122:125], v[224:227], v[94:97]
	v_mfma_f32_16x16x32_f16 v[70:73], v[122:125], v[228:231], v[70:73]
	s_waitcnt vmcnt(13)
	v_mfma_f32_16x16x32_f16 v[54:57], v[156:159], v[180:183], v[54:57]
	v_mfma_f32_16x16x32_f16 v[74:77], v[156:159], v[220:223], v[74:77]
	v_mfma_f32_16x16x32_f16 v[90:93], v[156:159], v[224:227], v[90:93]
	v_mfma_f32_16x16x32_f16 v[62:65], v[156:159], v[228:231], v[62:65]
	s_waitcnt vmcnt(12)
	v_mfma_f32_16x16x32_f16 v[38:41], v[160:163], v[180:183], v[38:41]
	buffer_load_dwordx4 v[94:97], v147, s[16:19], s8 offen
	buffer_load_dwordx4 v[122:125], v148, s[16:19], s8 offen
	buffer_load_dwordx4 v[156:159], v149, s[16:19], s8 offen
	buffer_load_dwordx4 v[180:183], v150, s[16:19], s8 offen
	v_mfma_f32_16x16x32_f16 v[42:45], v[160:163], v[220:223], v[42:45]
	v_mfma_f32_16x16x32_f16 v[46:49], v[160:163], v[224:227], v[46:49]
	v_mfma_f32_16x16x32_f16 v[34:37], v[160:163], v[228:231], v[34:37]
	v_add_u32_e32 v98, s73, v98
	ds_read_b128 v[160:163], v98
	ds_read_b128 v[220:223], v98 offset:16384
	ds_read_b128 v[224:227], v98 offset:32768
	ds_read_b128 v[228:231], v98 offset:49152
	s_add_i32 s8, s22, s42
	s_waitcnt vmcnt(15) lgkmcnt(7)
	v_mfma_f32_16x16x32_f16 v[164:167], v[66:69], v[188:191], v[164:167]
	s_waitcnt lgkmcnt(6)
	v_mfma_f32_16x16x32_f16 v[168:171], v[66:69], v[208:211], v[168:171]
	s_waitcnt lgkmcnt(5)
	v_mfma_f32_16x16x32_f16 v[172:175], v[66:69], v[212:215], v[172:175]
	s_waitcnt lgkmcnt(4)
	v_mfma_f32_16x16x32_f16 v[66:69], v[66:69], v[216:219], v[78:81]
	s_waitcnt vmcnt(14)
	v_mfma_f32_16x16x32_f16 v[58:61], v[192:195], v[188:191], v[58:61]
	v_mfma_f32_16x16x32_f16 v[78:81], v[192:195], v[208:211], v[82:85]
	v_mfma_f32_16x16x32_f16 v[82:85], v[192:195], v[212:215], v[86:89]
	v_mfma_f32_16x16x32_f16 v[70:73], v[192:195], v[216:219], v[70:73]
	s_waitcnt vmcnt(13)
	v_mfma_f32_16x16x32_f16 v[54:57], v[196:199], v[188:191], v[54:57]
	v_mfma_f32_16x16x32_f16 v[74:77], v[196:199], v[208:211], v[74:77]
	v_mfma_f32_16x16x32_f16 v[86:89], v[196:199], v[212:215], v[90:93]
	v_mfma_f32_16x16x32_f16 v[62:65], v[196:199], v[216:219], v[62:65]
	s_waitcnt vmcnt(12)
	v_mfma_f32_16x16x32_f16 v[38:41], v[200:203], v[188:191], v[38:41]
	buffer_load_dwordx4 v[90:93], v147, s[16:19], s8 offen
	buffer_load_dwordx4 v[188:191], v148, s[16:19], s8 offen
	buffer_load_dwordx4 v[192:195], v149, s[16:19], s8 offen
	buffer_load_dwordx4 v[196:199], v150, s[16:19], s8 offen
	v_mfma_f32_16x16x32_f16 v[42:45], v[200:203], v[208:211], v[42:45]
	v_mfma_f32_16x16x32_f16 v[46:49], v[200:203], v[212:215], v[46:49]
	v_mfma_f32_16x16x32_f16 v[34:37], v[200:203], v[216:219], v[34:37]
	v_add_u32_e32 v99, s74, v99
	ds_read_b128 v[200:203], v99
	ds_read_b128 v[208:211], v99 offset:16384
	ds_read_b128 v[212:215], v99 offset:32768
	ds_read_b128 v[216:219], v99 offset:49152
	s_add_i32 s8, s22, s43
	s_waitcnt vmcnt(15) lgkmcnt(7)
	v_mfma_f32_16x16x32_f16 v[164:167], v[50:53], v[160:163], v[164:167]
	s_waitcnt lgkmcnt(6)
	v_mfma_f32_16x16x32_f16 v[168:171], v[50:53], v[220:223], v[168:171]
	s_waitcnt lgkmcnt(5)
	v_mfma_f32_16x16x32_f16 v[172:175], v[50:53], v[224:227], v[172:175]
	s_waitcnt lgkmcnt(4)
	v_mfma_f32_16x16x32_f16 v[50:53], v[50:53], v[228:231], v[66:69]
	s_waitcnt vmcnt(14)
	v_mfma_f32_16x16x32_f16 v[58:61], v[140:143], v[160:163], v[58:61]
	v_mfma_f32_16x16x32_f16 v[66:69], v[140:143], v[220:223], v[78:81]
	v_mfma_f32_16x16x32_f16 v[78:81], v[140:143], v[224:227], v[82:85]
	v_mfma_f32_16x16x32_f16 v[70:73], v[140:143], v[228:231], v[70:73]
	s_waitcnt vmcnt(13)
	v_mfma_f32_16x16x32_f16 v[54:57], v[152:155], v[160:163], v[54:57]
	v_mfma_f32_16x16x32_f16 v[74:77], v[152:155], v[220:223], v[74:77]
	v_mfma_f32_16x16x32_f16 v[82:85], v[152:155], v[224:227], v[86:89]
	v_mfma_f32_16x16x32_f16 v[62:65], v[152:155], v[228:231], v[62:65]
	s_waitcnt vmcnt(12)
	v_mfma_f32_16x16x32_f16 v[38:41], v[176:179], v[160:163], v[38:41]
	buffer_load_dwordx4 v[86:89], v147, s[16:19], s8 offen
	buffer_load_dwordx4 v[140:143], v148, s[16:19], s8 offen
	buffer_load_dwordx4 v[152:155], v149, s[16:19], s8 offen
	buffer_load_dwordx4 v[160:163], v150, s[16:19], s8 offen
	v_mfma_f32_16x16x32_f16 v[42:45], v[176:179], v[220:223], v[42:45]
	v_mfma_f32_16x16x32_f16 v[46:49], v[176:179], v[224:227], v[46:49]
	v_mfma_f32_16x16x32_f16 v[34:37], v[176:179], v[228:231], v[34:37]
	v_add_u32_e32 v100, s75, v100
	ds_read_b128 v[176:179], v100
	ds_read_b128 v[220:223], v100 offset:16384
	ds_read_b128 v[224:227], v100 offset:32768
	ds_read_b128 v[228:231], v100 offset:49152
	s_add_i32 s8, s22, s44
	s_waitcnt vmcnt(15) lgkmcnt(7)
	v_mfma_f32_16x16x32_f16 v[164:167], v[126:129], v[200:203], v[164:167]
	s_waitcnt lgkmcnt(6)
	v_mfma_f32_16x16x32_f16 v[168:171], v[126:129], v[208:211], v[168:171]
	s_waitcnt lgkmcnt(5)
	v_mfma_f32_16x16x32_f16 v[172:175], v[126:129], v[212:215], v[172:175]
	s_waitcnt lgkmcnt(4)
	v_mfma_f32_16x16x32_f16 v[50:53], v[126:129], v[216:219], v[50:53]
	s_waitcnt vmcnt(14)
	v_mfma_f32_16x16x32_f16 v[58:61], v[136:139], v[200:203], v[58:61]
	v_mfma_f32_16x16x32_f16 v[66:69], v[136:139], v[208:211], v[66:69]
	v_mfma_f32_16x16x32_f16 v[78:81], v[136:139], v[212:215], v[78:81]
	v_mfma_f32_16x16x32_f16 v[70:73], v[136:139], v[216:219], v[70:73]
	s_waitcnt vmcnt(13)
	v_mfma_f32_16x16x32_f16 v[54:57], v[184:187], v[200:203], v[54:57]
	v_mfma_f32_16x16x32_f16 v[74:77], v[184:187], v[208:211], v[74:77]
	v_mfma_f32_16x16x32_f16 v[82:85], v[184:187], v[212:215], v[82:85]
	v_mfma_f32_16x16x32_f16 v[62:65], v[184:187], v[216:219], v[62:65]
	s_waitcnt vmcnt(12)
	v_mfma_f32_16x16x32_f16 v[38:41], v[204:207], v[200:203], v[38:41]
	buffer_load_dwordx4 v[126:129], v147, s[16:19], s8 offen
	buffer_load_dwordx4 v[136:139], v148, s[16:19], s8 offen
	buffer_load_dwordx4 v[184:187], v149, s[16:19], s8 offen
	buffer_load_dwordx4 v[200:203], v150, s[16:19], s8 offen
	v_mfma_f32_16x16x32_f16 v[42:45], v[204:207], v[208:211], v[42:45]
	v_mfma_f32_16x16x32_f16 v[46:49], v[204:207], v[212:215], v[46:49]
	v_mfma_f32_16x16x32_f16 v[34:37], v[204:207], v[216:219], v[34:37]
	v_add_u32_e32 v111, s76, v111
	ds_read_b128 v[204:207], v111
	ds_read_b128 v[208:211], v111 offset:16384
	ds_read_b128 v[212:215], v111 offset:32768
	ds_read_b128 v[216:219], v111 offset:49152
	s_add_i32 s8, s22, s45
	s_waitcnt vmcnt(15) lgkmcnt(7)
	v_mfma_f32_16x16x32_f16 v[164:167], v[94:97], v[176:179], v[164:167]
	s_waitcnt lgkmcnt(6)
	v_mfma_f32_16x16x32_f16 v[168:171], v[94:97], v[220:223], v[168:171]
	s_waitcnt vmcnt(14)
	v_mfma_f32_16x16x32_f16 v[58:61], v[122:125], v[176:179], v[58:61]
	v_mfma_f32_16x16x32_f16 v[66:69], v[122:125], v[220:223], v[66:69]
	s_waitcnt lgkmcnt(5)
	v_mfma_f32_16x16x32_f16 v[78:81], v[122:125], v[224:227], v[78:81]
	s_waitcnt lgkmcnt(4)
	v_mfma_f32_16x16x32_f16 v[70:73], v[122:125], v[228:231], v[70:73]
	s_waitcnt vmcnt(13)
	v_mfma_f32_16x16x32_f16 v[54:57], v[156:159], v[176:179], v[54:57]
	v_mfma_f32_16x16x32_f16 v[74:77], v[156:159], v[220:223], v[74:77]
	v_mfma_f32_16x16x32_f16 v[82:85], v[156:159], v[224:227], v[82:85]
	v_mfma_f32_16x16x32_f16 v[62:65], v[156:159], v[228:231], v[62:65]
	s_waitcnt vmcnt(12)
	v_mfma_f32_16x16x32_f16 v[38:41], v[180:183], v[176:179], v[38:41]
	v_mfma_f32_16x16x32_f16 v[42:45], v[180:183], v[220:223], v[42:45]
	buffer_load_dwordx4 v[122:125], v147, s[16:19], s8 offen
	buffer_load_dwordx4 v[156:159], v148, s[16:19], s8 offen
	buffer_load_dwordx4 v[176:179], v149, s[16:19], s8 offen
	buffer_load_dwordx4 v[220:223], v150, s[16:19], s8 offen
	v_mfma_f32_16x16x32_f16 v[50:53], v[94:97], v[228:231], v[50:53]
	v_mfma_f32_16x16x32_f16 v[46:49], v[180:183], v[224:227], v[46:49]
	v_mfma_f32_16x16x32_f16 v[34:37], v[180:183], v[228:231], v[34:37]
	v_mfma_f32_16x16x32_f16 v[172:175], v[94:97], v[224:227], v[172:175]
	v_add_u32_e32 v98, s77, v98
	ds_read_b128 v[94:97], v98
	ds_read_b128 v[180:183], v98 offset:16384
	ds_read_b128 v[224:227], v98 offset:32768
	ds_read_b128 v[228:231], v98 offset:49152
	s_add_i32 s8, s22, s46
	s_waitcnt vmcnt(15) lgkmcnt(7)
	v_mfma_f32_16x16x32_f16 v[164:167], v[90:93], v[204:207], v[164:167]
	s_waitcnt lgkmcnt(6)
	v_mfma_f32_16x16x32_f16 v[168:171], v[90:93], v[208:211], v[168:171]
	s_waitcnt lgkmcnt(5)
	v_mfma_f32_16x16x32_f16 v[172:175], v[90:93], v[212:215], v[172:175]
	s_waitcnt lgkmcnt(4)
	v_mfma_f32_16x16x32_f16 v[90:93], v[90:93], v[216:219], v[50:53]
	s_waitcnt vmcnt(14)
	v_mfma_f32_16x16x32_f16 v[232:235], v[188:191], v[204:207], v[58:61]
	v_mfma_f32_16x16x32_f16 v[66:69], v[188:191], v[208:211], v[66:69]
	v_mfma_f32_16x16x32_f16 v[78:81], v[188:191], v[212:215], v[78:81]
	v_mfma_f32_16x16x32_f16 v[70:73], v[188:191], v[216:219], v[70:73]
	s_waitcnt vmcnt(13)
	v_mfma_f32_16x16x32_f16 v[188:191], v[192:195], v[204:207], v[54:57]
	v_mfma_f32_16x16x32_f16 v[74:77], v[192:195], v[208:211], v[74:77]
	v_mfma_f32_16x16x32_f16 v[82:85], v[192:195], v[212:215], v[82:85]
	v_mfma_f32_16x16x32_f16 v[62:65], v[192:195], v[216:219], v[62:65]
	s_waitcnt vmcnt(12)
	v_mfma_f32_16x16x32_f16 v[192:195], v[196:199], v[204:207], v[38:41]
	buffer_load_dwordx4 v[58:61], v147, s[16:19], s8 offen
	buffer_load_dwordx4 v[54:57], v148, s[16:19], s8 offen
	buffer_load_dwordx4 v[50:53], v149, s[16:19], s8 offen
	buffer_load_dwordx4 v[38:41], v150, s[16:19], s8 offen
	v_mfma_f32_16x16x32_f16 v[42:45], v[196:199], v[208:211], v[42:45]
	v_mfma_f32_16x16x32_f16 v[46:49], v[196:199], v[212:215], v[46:49]
	v_mfma_f32_16x16x32_f16 v[196:199], v[196:199], v[216:219], v[34:37]
	v_add_u32_e32 v99, s78, v99
	ds_read_b128 v[204:207], v99
	ds_read_b128 v[208:211], v99 offset:16384
	ds_read_b128 v[212:215], v99 offset:32768
	ds_read_b128 v[216:219], v99 offset:49152
	s_add_i32 s8, s22, s47
	s_waitcnt vmcnt(15) lgkmcnt(7)
	v_mfma_f32_16x16x32_f16 v[164:167], v[86:89], v[94:97], v[164:167]
	s_waitcnt lgkmcnt(6)
	v_mfma_f32_16x16x32_f16 v[168:171], v[86:89], v[180:183], v[168:171]
	s_waitcnt lgkmcnt(5)
	v_mfma_f32_16x16x32_f16 v[172:175], v[86:89], v[224:227], v[172:175]
	s_waitcnt lgkmcnt(4)
	v_mfma_f32_16x16x32_f16 v[86:89], v[86:89], v[228:231], v[90:93]
	s_waitcnt vmcnt(14)
	v_mfma_f32_16x16x32_f16 v[232:235], v[140:143], v[94:97], v[232:235]
	v_mfma_f32_16x16x32_f16 v[66:69], v[140:143], v[180:183], v[66:69]
	v_mfma_f32_16x16x32_f16 v[236:239], v[140:143], v[224:227], v[78:81]
	v_mfma_f32_16x16x32_f16 v[70:73], v[140:143], v[228:231], v[70:73]
	s_waitcnt vmcnt(13)
	v_mfma_f32_16x16x32_f16 v[140:143], v[152:155], v[94:97], v[188:191]
	v_mfma_f32_16x16x32_f16 v[74:77], v[152:155], v[180:183], v[74:77]
	v_mfma_f32_16x16x32_f16 v[82:85], v[152:155], v[224:227], v[82:85]
	v_mfma_f32_16x16x32_f16 v[62:65], v[152:155], v[228:231], v[62:65]
	s_waitcnt vmcnt(12)
	v_mfma_f32_16x16x32_f16 v[152:155], v[160:163], v[94:97], v[192:195]
	buffer_load_dwordx4 v[94:97], v147, s[16:19], s8 offen
	buffer_load_dwordx4 v[90:93], v148, s[16:19], s8 offen
	buffer_load_dwordx4 v[78:81], v149, s[16:19], s8 offen
	buffer_load_dwordx4 v[34:37], v150, s[16:19], s8 offen
	v_mfma_f32_16x16x32_f16 v[42:45], v[160:163], v[180:183], v[42:45]
	v_mfma_f32_16x16x32_f16 v[46:49], v[160:163], v[224:227], v[46:49]
	v_mfma_f32_16x16x32_f16 v[160:163], v[160:163], v[228:231], v[196:199]
	v_add_u32_e32 v100, s79, v100
	ds_read_b128 v[180:183], v100
	ds_read_b128 v[188:191], v100 offset:16384
	ds_read_b128 v[192:195], v100 offset:32768
	ds_read_b128 v[196:199], v100 offset:49152
	s_add_i32 s8, s22, s48
	s_waitcnt vmcnt(15) lgkmcnt(7)
	v_mfma_f32_16x16x32_f16 v[164:167], v[126:129], v[204:207], v[164:167]
	s_waitcnt lgkmcnt(6)
	v_mfma_f32_16x16x32_f16 v[168:171], v[126:129], v[208:211], v[168:171]
	s_waitcnt lgkmcnt(5)
	v_mfma_f32_16x16x32_f16 v[172:175], v[126:129], v[212:215], v[172:175]
	s_waitcnt lgkmcnt(4)
	v_mfma_f32_16x16x32_f16 v[86:89], v[126:129], v[216:219], v[86:89]
	s_waitcnt vmcnt(14)
	v_mfma_f32_16x16x32_f16 v[126:129], v[136:139], v[204:207], v[232:235]
	v_mfma_f32_16x16x32_f16 v[66:69], v[136:139], v[208:211], v[66:69]
	v_mfma_f32_16x16x32_f16 v[224:227], v[136:139], v[212:215], v[236:239]
	v_mfma_f32_16x16x32_f16 v[136:139], v[136:139], v[216:219], v[70:73]
	s_waitcnt vmcnt(13)
	v_mfma_f32_16x16x32_f16 v[140:143], v[184:187], v[204:207], v[140:143]
	v_mfma_f32_16x16x32_f16 v[74:77], v[184:187], v[208:211], v[74:77]
	v_mfma_f32_16x16x32_f16 v[228:231], v[184:187], v[212:215], v[82:85]
	v_mfma_f32_16x16x32_f16 v[184:187], v[184:187], v[216:219], v[62:65]
	s_waitcnt vmcnt(12)
	v_mfma_f32_16x16x32_f16 v[152:155], v[200:203], v[204:207], v[152:155]
	v_mfma_f32_16x16x32_f16 v[204:207], v[200:203], v[208:211], v[42:45]
	buffer_load_dwordx4 v[82:85], v147, s[16:19], s8 offen
	buffer_load_dwordx4 v[70:73], v148, s[16:19], s8 offen
	buffer_load_dwordx4 v[62:65], v149, s[16:19], s8 offen
	buffer_load_dwordx4 v[42:45], v150, s[16:19], s8 offen
	v_mfma_f32_16x16x32_f16 v[46:49], v[200:203], v[212:215], v[46:49]
	v_mfma_f32_16x16x32_f16 v[160:163], v[200:203], v[216:219], v[160:163]
	v_add_u32_e32 v0, 0x1ac00, v104
	ds_read_b128 v[240:243], v0
	ds_read_b128 v[244:247], v0 offset:16
	s_waitcnt vmcnt(12) lgkmcnt(5)
	v_mfma_f32_16x16x32_f16 v[164:167], v[122:125], v[180:183], v[164:167]
	v_mfma_f32_16x16x32_f16 v[126:129], v[156:159], v[180:183], v[126:129]
	v_mfma_f32_16x16x32_f16 v[140:143], v[176:179], v[180:183], v[140:143]
	v_mfma_f32_16x16x32_f16 v[152:155], v[220:223], v[180:183], v[152:155]
	s_waitcnt lgkmcnt(4)
	v_mfma_f32_16x16x32_f16 v[168:171], v[122:125], v[188:191], v[168:171]
	v_mfma_f32_16x16x32_f16 v[208:211], v[156:159], v[188:191], v[66:69]
	v_mfma_f32_16x16x32_f16 v[212:215], v[176:179], v[188:191], v[74:77]
	v_mfma_f32_16x16x32_f16 v[204:207], v[220:223], v[188:191], v[204:207]
	s_waitcnt lgkmcnt(3)
	v_mfma_f32_16x16x32_f16 v[172:175], v[122:125], v[192:195], v[172:175]
	v_cvt_pk_f16_f32 v232, v164, v165
	v_cvt_pk_f16_f32 v233, v166, v167
	v_pk_max_f16 v232, v232, 0
	v_pk_max_f16 v233, v233, 0
	v_mfma_f32_16x16x32_f16 v[224:227], v[156:159], v[192:195], v[224:227]
	v_cvt_pk_f16_f32 v234, v126, v127
	v_cvt_pk_f16_f32 v235, v128, v129
	v_pk_max_f16 v234, v234, 0
	v_pk_max_f16 v235, v235, 0
	v_mfma_f32_16x16x32_f16 v[228:231], v[176:179], v[192:195], v[228:231]
	v_cvt_pk_f16_f32 v236, v140, v141
	v_cvt_pk_f16_f32 v237, v142, v143
	v_pk_max_f16 v236, v236, 0
	v_pk_max_f16 v237, v237, 0
	v_mfma_f32_16x16x32_f16 v[216:219], v[220:223], v[192:195], v[46:49]
	v_cvt_pk_f16_f32 v238, v152, v153
	v_cvt_pk_f16_f32 v239, v154, v155
	v_pk_max_f16 v238, v238, 0
	v_pk_max_f16 v239, v239, 0
	s_waitcnt lgkmcnt(2)
	v_mfma_f32_16x16x32_f16 v[200:203], v[122:125], v[196:199], v[86:89]
	v_cvt_pk_f16_f32 v180, v168, v169
	v_cvt_pk_f16_f32 v181, v170, v171
	v_pk_max_f16 v180, v180, 0
	v_pk_max_f16 v181, v181, 0
	s_add_i32 s8, s22, s49
	buffer_load_dwordx4 v[86:89], v147, s[16:19], s8 offen
	buffer_load_dwordx4 v[74:77], v148, s[16:19], s8 offen
	buffer_load_dwordx4 v[66:69], v149, s[16:19], s8 offen
	buffer_load_dwordx4 v[46:49], v150, s[16:19], s8 offen
	v_mfma_f32_16x16x32_f16 v[136:139], v[156:159], v[196:199], v[136:139]
	v_cvt_pk_f16_f32 v182, v208, v209
	v_cvt_pk_f16_f32 v183, v210, v211
	v_pk_max_f16 v182, v182, 0
	v_pk_max_f16 v183, v183, 0
	s_waitcnt lgkmcnt(1)
	v_mfma_f32_16x16x32_f16 v[252:255], v[240:243], v[232:235], 0
	v_cvt_pk_f16_f32 v232, v172, v173
	v_cvt_pk_f16_f32 v233, v174, v175
	v_pk_max_f16 v232, v232, 0
	v_pk_max_f16 v233, v233, 0
	v_mfma_f32_16x16x32_f16 v[184:187], v[176:179], v[196:199], v[184:187]
	v_cvt_pk_f16_f32 v188, v212, v213
	v_cvt_pk_f16_f32 v189, v214, v215
	v_pk_max_f16 v188, v188, 0
	v_pk_max_f16 v189, v189, 0
	s_waitcnt lgkmcnt(0)
	v_mfma_f32_16x16x32_f16 v[252:255], v[244:247], v[236:239], v[252:255]
	ds_read_u16 v102, v114
	ds_read_u16 v103, v114 offset:512
	ds_read_u16 v115, v114 offset:1024
	ds_read_u16 v116, v114 offset:1536
	v_cvt_pk_f16_f32 v234, v224, v225
	v_cvt_pk_f16_f32 v235, v226, v227
	v_pk_max_f16 v234, v234, 0
	v_pk_max_f16 v235, v235, 0
	v_mfma_f32_16x16x32_f16 v[160:163], v[220:223], v[196:199], v[160:163]
	v_cvt_pk_f16_f32 v190, v204, v205
	v_cvt_pk_f16_f32 v191, v206, v207
	v_pk_max_f16 v190, v190, 0
	v_pk_max_f16 v191, v191, 0
	v_mfma_f32_16x16x32_f16 v[192:195], v[240:243], v[180:183], 0
	v_cvt_pk_f16_f32 v236, v228, v229
	v_cvt_pk_f16_f32 v237, v230, v231
	v_pk_max_f16 v236, v236, 0
	v_pk_max_f16 v237, v237, 0
	v_mfma_f32_16x16x32_f16 v[192:195], v[244:247], v[188:191], v[192:195]
	v_cvt_pk_f16_f32 v238, v216, v217
	v_cvt_pk_f16_f32 v239, v218, v219
	v_pk_max_f16 v238, v238, 0
	v_pk_max_f16 v239, v239, 0
	v_cvt_pk_f16_f32 v180, v200, v201
	v_cvt_pk_f16_f32 v181, v202, v203
	v_pk_max_f16 v180, v180, 0
	v_pk_max_f16 v181, v181, 0
	v_mfma_f32_16x16x32_f16 v[196:199], v[240:243], v[232:235], 0
	v_cvt_pk_f16_f32 v182, v136, v137
	v_cvt_pk_f16_f32 v183, v138, v139
	v_pk_max_f16 v182, v182, 0
	v_pk_max_f16 v183, v183, 0
	v_mfma_f32_16x16x32_f16 v[196:199], v[244:247], v[236:239], v[196:199]
	v_cvt_pk_f16_f32 v188, v184, v185
	v_cvt_pk_f16_f32 v189, v186, v187
	v_mfma_f32_16x16x32_f16 v[122:125], v[240:243], v[180:183], 0
	v_pk_max_f16 v188, v188, 0
	v_pk_max_f16 v189, v189, 0
	v_cvt_pk_f16_f32 v190, v160, v161
	v_cvt_pk_f16_f32 v191, v162, v163
	v_pk_max_f16 v190, v190, 0
	v_pk_max_f16 v191, v191, 0
	s_nop 1
	v_mfma_f32_16x16x32_f16 v[122:125], v[244:247], v[188:191], v[122:125]
	v_add_u32_e32 v145, 0x12c00, v105
	v_cndmask_b32_e64 v0, v252, v192, s[2:3]
	v_cndmask_b32_e64 v0, v0, v196, s[0:1]
	s_waitcnt vmcnt(16)
	v_cndmask_b32_e64 v1, v30, v134, s[0:1]
	v_bfi_b32 v30, s10, v1, v30
	v_perm_b32 v1, v22, v134, s24
	v_cndmask_b32_e64 v22, v22, v1, s[0:1]
	v_cndmask_b32_e64 v0, v0, v122, s[26:27]
	ds_write_b32 v112, v0
	v_bfi_b32 v1, s10, v135, v18
	v_perm_b32 v121, v10, v135, s24
	v_cndmask_b32_e64 v18, v18, v1, s[0:1]
	v_cndmask_b32_e64 v10, v10, v121, s[0:1]
	s_add_i32 s22, s22, 0x80000
	s_add_i32 s11, s11, 1
	s_add_u32 s12, s12, 4
	s_addc_u32 s13, s13, 0
	v_add_u32_e32 v104, 0x400, v104
	v_add_u32_e32 v105, 0x800, v105
	v_add_u32_e32 v114, 2, v114
	s_cmp_eq_u32 s22, 0x898000
	s_waitcnt lgkmcnt(0)
	s_barrier
	ds_read_b128 v[232:235], v113
	ds_read_b128 v[236:239], v113 offset:1024
	ds_read_b128 v[240:243], v145 offset:2048
	ds_read_b128 v[244:247], v145 offset:2064
	ds_read_b128 v[248:251], v145 offset:2080
	ds_read_b128 v[252:255], v145 offset:2096
	s_waitcnt lgkmcnt(4)
	v_add_f32_e32 v0, v232, v233
	v_add_f32_e32 v1, v234, v235
	v_add_f32_e32 v121, v236, v237
	v_add_f32_e32 v144, v238, v239
	v_add_f32_e32 v0, v0, v1
	v_add_f32_e32 v121, v121, v144
	v_add_f32_e32 v0, v0, v121
	v_add_f32_e32 v0, s30, v0
	v_cvt_f16_f32_e32 v1, v0
	v_cvt_f16_f32_e32 v121, v0
	ds_write_b32 v106, v0
	v_add_u32_e32 v106, 4, v106
	v_permlane16_swap_b32_e32 v1, v121
	s_cbranch_scc0 .LBB1_4
